# attention unit epilogue: the 13 half-wave sum chains (5 ds_swizzle round trips each) through DPP + v_permlane16_swap, code size kept with s_nop so every hot loop stays at its offset; bit-identical
# speedup vs baseline: 1.0005x; 1.0005x over previous
; __device__ __forceinline__ float half_sum32(float v) { v += swz_xor_f<1>(v); v += swz_xor_f<2>(v); v += swz_xor_f<4>(v); v += swz_xor_f<8>(v); v += swz_xor_f<16>(v); return v; }
; __device__ __forceinline__ int crow(int r, int hi) { return (r & 3) + 8 * (r >> 2) + 4 * hi; }
; __device__ __forceinline__ void attn_unit_f8(const bf16_t* __restrict__ Q, const bf16_t* __restrict__ Kb, const unsigned char* __restrict__ V8, bf16_t* __restrict__ O, ...
;     ...
;   if (cq == 0) {
;     float ss[16];
; #pragma unroll
;     for (int r = 0; r < 16; ++r) { float s = 0.f;
; #pragma unroll
;       for (int d0 = 0; d0 < 4; ++d0) { const float v = o[d0][r] * rli[r] - lam * xb[crow(r, hi) * 128 + d0 * 32 + r32]; o[d0][r] = v; s += v * v; }
;       ss[r] = s; }
; #pragma unroll
;     for (int r = 0; r < 16; ++r) { float s = half_sum32(ss[r]); ss[r] = __builtin_amdgcn_rsqf(s * (1.0f / 128.0f) + LN_EPS) * (1.0f - LAM_INIT); }
;     float gsub[4];
; #pragma unroll
;     for (int d0 = 0; d0 < 4; ++d0) gsub[d0] = subg[d0 * 32 + r32];
;     unsigned char* Ow = (unsigned char*)O + (size_t)(qrow0 + wq * QBLK) * DM + h * 128;
.LBB0_1359:
	s_waitcnt lgkmcnt(0)
	s_barrier
	s_andn2_b64 vcc, exec, s[80:81]
	s_cbranch_vccnz .LBB0_1290
	ds_read2_b32 v[66:67], v90 offset1:32
	ds_read2_b32 v[68:69], v90 offset0:64 offset1:96
	s_lshl_b32 s0, s50, 5
	s_or_b32 s0, s0, s25
	s_ashr_i32 s1, s0, 31
	s_waitcnt lgkmcnt(1)
	v_mul_f32_e32 v66, v197, v66
	v_fma_f32 v66, v2, v88, -v66
	v_mul_f32_e32 v2, v197, v67
	s_waitcnt lgkmcnt(0)
	v_mul_f32_e32 v67, v197, v68
	v_fma_f32 v67, v34, v88, -v67
	v_mul_f32_e32 v34, v197, v69
	ds_read2_b32 v[68:69], v90 offset0:128 offset1:160
	v_fma_f32 v34, v50, v88, -v34
	v_fma_f32 v18, v18, v88, -v2
	v_mul_f32_e32 v2, v18, v18
	v_fmac_f32_e32 v2, v66, v66
	s_waitcnt lgkmcnt(0)
	v_mul_f32_e32 v50, v197, v68
	v_fma_f32 v50, v3, v87, -v50
	v_mul_f32_e32 v3, v197, v69
	ds_read2_b32 v[68:69], v90 offset0:192 offset1:224
	v_fma_f32 v19, v19, v87, -v3
	v_fmac_f32_e32 v2, v67, v67
	v_fmac_f32_e32 v2, v34, v34
	v_mul_f32_e32 v80, v19, v19
	s_waitcnt lgkmcnt(0)
	v_mul_f32_e32 v3, v197, v68
	v_fma_f32 v68, v35, v87, -v3
	v_mul_f32_e32 v3, v197, v69
	v_fma_f32 v35, v51, v87, -v3
	v_add_u32_e32 v3, 0x400, v90
	ds_read2_b32 v[70:71], v3 offset1:32
	v_fmac_f32_e32 v80, v50, v50
	v_fmac_f32_e32 v80, v68, v68
	v_fmac_f32_e32 v80, v35, v35
	s_lshl_b64 s[0:1], s[0:1], 10
	s_waitcnt lgkmcnt(0)
	v_mul_f32_e32 v51, v197, v70
	v_fma_f32 v51, v4, v86, -v51
	v_mul_f32_e32 v4, v197, v71
	ds_read2_b32 v[70:71], v3 offset0:64 offset1:96
	v_fma_f32 v4, v20, v86, -v4
	v_mul_f32_e32 v81, v4, v4
	v_fmac_f32_e32 v81, v51, v51
	s_add_u32 s0, s16, s0
	s_waitcnt lgkmcnt(0)
	v_mul_f32_e32 v20, v197, v70
	v_fma_f32 v69, v36, v86, -v20
	v_mul_f32_e32 v20, v197, v71
	ds_read2_b32 v[70:71], v3 offset0:128 offset1:160
	v_fma_f32 v36, v52, v86, -v20
	v_fmac_f32_e32 v81, v69, v69
	v_fmac_f32_e32 v81, v36, v36
	s_addc_u32 s1, s17, s1
	s_waitcnt lgkmcnt(0)
	v_mul_f32_e32 v20, v197, v70
	v_fma_f32 v52, v5, v85, -v20
	v_mul_f32_e32 v5, v197, v71
	v_fma_f32 v5, v21, v85, -v5
	ds_read2_b32 v[20:21], v3 offset0:192 offset1:224
	v_mul_f32_e32 v87, v5, v5
	v_fmac_f32_e32 v87, v52, v52
	s_add_u32 s0, s0, s18
	v_mov_b32_e32 v179, v1
	s_waitcnt lgkmcnt(0)
	v_mul_f32_e32 v3, v197, v20
	v_fma_f32 v70, v37, v85, -v3
	v_mul_f32_e32 v3, v197, v21
	v_fma_f32 v21, v53, v85, -v3
	v_add_u32_e32 v3, 0x1000, v90
	ds_read2_b32 v[88:89], v3 offset1:32
	ds_read2_b32 v[94:95], v3 offset0:64 offset1:96
	v_fmac_f32_e32 v87, v70, v70
	v_fmac_f32_e32 v87, v21, v21
	s_addc_u32 s1, s1, s19
	s_waitcnt lgkmcnt(1)
	v_mul_f32_e32 v20, v197, v88
	v_fma_f32 v53, v6, v84, -v20
	v_mul_f32_e32 v6, v197, v89
	v_fma_f32 v20, v22, v84, -v6
	s_waitcnt lgkmcnt(0)
	v_mul_f32_e32 v6, v197, v94
	v_fma_f32 v38, v38, v84, -v6
	v_mul_f32_e32 v6, v197, v95
	v_fma_f32 v22, v54, v84, -v6
	ds_read2_b32 v[84:85], v3 offset0:128 offset1:160
	v_mul_f32_e32 v88, v20, v20
	v_fmac_f32_e32 v88, v53, v53
	v_fmac_f32_e32 v88, v38, v38
	v_fmac_f32_e32 v88, v22, v22
	s_waitcnt lgkmcnt(0)
	v_mul_f32_e32 v6, v197, v84
	v_fma_f32 v54, v7, v82, -v6
	v_mul_f32_e32 v6, v197, v85
	ds_read2_b32 v[84:85], v3 offset0:192 offset1:224
	v_fma_f32 v7, v23, v82, -v6
	v_mul_f32_e32 v89, v7, v7
	v_fmac_f32_e32 v89, v54, v54
	v_lshlrev_b32_e32 v0, 12, v0
	s_waitcnt lgkmcnt(0)
	v_mul_f32_e32 v3, v197, v84
	v_fma_f32 v71, v39, v82, -v3
	v_mul_f32_e32 v3, v197, v85
	v_fma_f32 v37, v55, v82, -v3
	v_add_u32_e32 v3, 0x1400, v90
	ds_read2_b32 v[84:85], v3 offset1:32
	v_fmac_f32_e32 v89, v71, v71
	v_fmac_f32_e32 v89, v37, v37
	s_waitcnt lgkmcnt(0)
	v_mul_f32_e32 v6, v197, v84
	v_fma_f32 v55, v8, v83, -v6
	v_mul_f32_e32 v6, v197, v85
	ds_read2_b32 v[84:85], v3 offset0:64 offset1:96
	v_fma_f32 v23, v24, v83, -v6
	v_mul_f32_e32 v82, v23, v23
	v_fmac_f32_e32 v82, v55, v55
	s_waitcnt lgkmcnt(0)
	v_mul_f32_e32 v6, v197, v84
	v_fma_f32 v72, v40, v83, -v6
	v_mul_f32_e32 v6, v197, v85
	ds_read2_b32 v[84:85], v3 offset0:128 offset1:160
	v_fma_f32 v24, v56, v83, -v6
	v_fmac_f32_e32 v82, v72, v72
	v_fmac_f32_e32 v82, v24, v24
	s_waitcnt lgkmcnt(0)
	v_mul_f32_e32 v6, v197, v84
	v_fma_f32 v56, v9, v73, -v6
	v_mul_f32_e32 v6, v197, v85
	ds_read2_b32 v[84:85], v3 offset0:192 offset1:224
	v_fma_f32 v9, v25, v73, -v6
	v_add_u32_e32 v6, 0x2000, v90
	ds_read2_b32 v[94:95], v6 offset0:64 offset1:96
	v_mul_f32_e32 v83, v9, v9
	s_waitcnt lgkmcnt(1)
	v_mul_f32_e32 v3, v197, v84
	v_fma_f32 v41, v41, v73, -v3
	v_mul_f32_e32 v3, v197, v85
	ds_read2_b32 v[84:85], v6 offset1:32
	v_fma_f32 v39, v57, v73, -v3
	v_fmac_f32_e32 v83, v56, v56
	v_fmac_f32_e32 v83, v41, v41
	v_fmac_f32_e32 v83, v39, v39
	s_waitcnt lgkmcnt(0)
	v_mul_f32_e32 v3, v197, v84
	v_fma_f32 v73, v10, v74, -v3
	v_mul_f32_e32 v3, v197, v85
	v_fma_f32 v10, v26, v74, -v3
	v_mul_f32_e32 v3, v197, v94
	v_fma_f32 v57, v42, v74, -v3
	v_mul_f32_e32 v3, v197, v95
	ds_read2_b32 v[94:95], v6 offset0:128 offset1:160
	v_fma_f32 v26, v58, v74, -v3
	v_mul_f32_e32 v84, v10, v10
	v_fmac_f32_e32 v84, v73, v73
	v_fmac_f32_e32 v84, v57, v57
	s_waitcnt lgkmcnt(0)
	v_mul_f32_e32 v3, v197, v94
	v_fma_f32 v58, v11, v75, -v3
	v_mul_f32_e32 v3, v197, v95
	ds_read2_b32 v[94:95], v6 offset0:192 offset1:224
	v_fma_f32 v25, v27, v75, -v3
	v_fmac_f32_e32 v84, v26, v26
	v_mul_f32_e32 v3, v25, v25
	v_fmac_f32_e32 v3, v58, v58
	s_waitcnt lgkmcnt(0)
	v_mul_f32_e32 v6, v197, v94
	v_fma_f32 v74, v43, v75, -v6
	v_mul_f32_e32 v6, v197, v95
	v_fma_f32 v40, v59, v75, -v6
	v_add_u32_e32 v6, 0x2400, v90
	ds_read2_b32 v[42:43], v6 offset1:32
	ds_read2_b32 v[94:95], v6 offset0:128 offset1:160
	v_fmac_f32_e32 v3, v74, v74
	v_fmac_f32_e32 v3, v40, v40
	s_waitcnt lgkmcnt(1)
; __device__ __forceinline__ float half_sum32(float v) { v += swz_xor_f<1>(v); v += swz_xor_f<2>(v); v += swz_xor_f<4>(v); v += swz_xor_f<8>(v); v += swz_xor_f<16>(v); return v; }
; __device__ __forceinline__ int crow(int r, int hi) { return (r & 3) + 8 * (r >> 2) + 4 * hi; }
; __device__ __forceinline__ void attn_unit_f8(const bf16_t* __restrict__ Q, const bf16_t* __restrict__ Kb, const unsigned char* __restrict__ V8, bf16_t* __restrict__ O, ...
;     ...
;     for (int r = 0; r < 16; ++r) { float s = 0.f;
; #pragma unroll
;       for (int d0 = 0; d0 < 4; ++d0) { const float v = o[d0][r] * rli[r] - lam * xb[crow(r, hi) * 128 + d0 * 32 + r32]; o[d0][r] = v; s += v * v; }
;       ss[r] = s; }
; #pragma unroll
;     for (int r = 0; r < 16; ++r) { float s = half_sum32(ss[r]); ss[r] = __builtin_amdgcn_rsqf(s * (1.0f / 128.0f) + LN_EPS) * (1.0f - LAM_INIT); }
	v_mul_f32_e32 v8, v197, v42
	v_fma_f32 v59, v12, v76, -v8
	v_mul_f32_e32 v8, v197, v43
	ds_read2_b32 v[42:43], v6 offset0:64 offset1:96
	v_fma_f32 v27, v28, v76, -v8
	v_mul_f32_e32 v85, v27, v27
	v_fmac_f32_e32 v85, v59, v59
	s_waitcnt lgkmcnt(0)
	v_mul_f32_e32 v8, v197, v42
	v_fma_f32 v75, v44, v76, -v8
	v_mul_f32_e32 v8, v197, v43
	v_fma_f32 v42, v60, v76, -v8
	v_mul_f32_e32 v8, v197, v94
	v_fma_f32 v60, v13, v92, -v8
	ds_read2_b32 v[12:13], v6 offset0:192 offset1:224
	v_mul_f32_e32 v8, v197, v95
	v_fma_f32 v28, v29, v92, -v8
	v_fmac_f32_e32 v85, v75, v75
	v_fmac_f32_e32 v85, v42, v42
	s_waitcnt lgkmcnt(0)
	v_mul_f32_e32 v6, v197, v12
	v_fma_f32 v76, v45, v92, -v6
	v_mul_f32_e32 v6, v197, v13
	v_fma_f32 v44, v61, v92, -v6
	v_add_u32_e32 v6, 0x3000, v90
	ds_read2_b32 v[12:13], v6 offset1:32
	ds_read2_b32 v[94:95], v6 offset0:64 offset1:96
	v_mul_f32_e32 v86, v28, v28
	v_fmac_f32_e32 v86, v60, v60
	v_fmac_f32_e32 v86, v76, v76
	s_waitcnt lgkmcnt(1)
	v_mul_f32_e32 v8, v197, v12
	v_fma_f32 v61, v14, v93, -v8
	v_mul_f32_e32 v8, v197, v13
	v_fma_f32 v12, v30, v93, -v8
	s_waitcnt lgkmcnt(0)
	v_mul_f32_e32 v8, v197, v94
	v_fma_f32 v45, v46, v93, -v8
	v_mul_f32_e32 v8, v197, v95
	ds_read2_b32 v[94:95], v6 offset0:128 offset1:160
	v_fma_f32 v29, v62, v93, -v8
	v_fmac_f32_e32 v86, v44, v44
	v_mul_f32_e32 v92, v12, v12
	v_fmac_f32_e32 v92, v61, v61
	s_waitcnt lgkmcnt(0)
	v_mul_f32_e32 v8, v197, v94
	v_fma_f32 v43, v15, v91, -v8
	ds_read2_b32 v[14:15], v6 offset0:192 offset1:224
	v_mul_f32_e32 v8, v197, v95
	v_fma_f32 v13, v31, v91, -v8
	v_fmac_f32_e32 v92, v45, v45
	v_fmac_f32_e32 v92, v29, v29
	s_waitcnt lgkmcnt(0)
	v_mul_f32_e32 v6, v197, v14
	v_fma_f32 v46, v47, v91, -v6
	v_mul_f32_e32 v6, v197, v15
	v_fma_f32 v30, v63, v91, -v6
	v_add_u32_e32 v6, 0x3400, v90
	ds_read2_b32 v[14:15], v6 offset1:32
	ds_read2_b32 v[62:63], v6 offset0:64 offset1:96
	v_mul_f32_e32 v93, v13, v13
	v_fmac_f32_e32 v93, v43, v43
	v_fmac_f32_e32 v93, v46, v46
	s_waitcnt lgkmcnt(1)
	v_mul_f32_e32 v8, v197, v14
	v_fma_f32 v31, v16, v79, -v8
	v_mul_f32_e32 v8, v197, v15
	v_fma_f32 v15, v32, v79, -v8
	s_waitcnt lgkmcnt(0)
	v_mul_f32_e32 v8, v197, v62
	v_fma_f32 v32, v48, v79, -v8
	v_mul_f32_e32 v8, v197, v63
	ds_read2_b32 v[62:63], v6 offset0:128 offset1:160
	v_fma_f32 v16, v64, v79, -v8
	v_fmac_f32_e32 v93, v30, v30
	v_mul_f32_e32 v90, v15, v15
	v_fmac_f32_e32 v90, v31, v31
	s_waitcnt lgkmcnt(0)
	v_mul_f32_e32 v8, v197, v62
	v_fma_f32 v14, v17, v78, -v8
	v_mul_f32_e32 v8, v197, v63
	v_fma_f32 v11, v33, v78, -v8
	ds_swizzle_b32 v33, v2 offset:swizzle(SWAP,1)
	ds_read2_b32 v[62:63], v6 offset0:192 offset1:224
	v_fmac_f32_e32 v90, v32, v32
	v_fmac_f32_e32 v90, v16, v16
	v_mul_f32_e32 v17, v11, v11
	s_waitcnt lgkmcnt(1)
	v_add_f32_e32 v2, v2, v33
	ds_swizzle_b32 v33, v2 offset:swizzle(SWAP,2)
	s_waitcnt lgkmcnt(1)
	v_mul_f32_e32 v6, v197, v62
	v_fma_f32 v8, v49, v78, -v6
	v_mul_f32_e32 v6, v197, v63
	v_fma_f32 v6, v65, v78, -v6
	s_waitcnt lgkmcnt(0)
	v_add_f32_e32 v2, v2, v33
	ds_swizzle_b32 v33, v2 offset:swizzle(SWAP,4)
	v_fmac_f32_e32 v17, v14, v14
	v_fmac_f32_e32 v17, v8, v8
	v_fmac_f32_e32 v17, v6, v6
	s_waitcnt lgkmcnt(0)
	v_add_f32_e32 v2, v2, v33
	ds_swizzle_b32 v33, v2 offset:swizzle(SWAP,8)
	s_waitcnt lgkmcnt(0)
	v_add_f32_e32 v2, v2, v33
	ds_swizzle_b32 v33, v2 offset:swizzle(SWAP,16)
	s_waitcnt lgkmcnt(0)
	v_add_f32_e32 v2, v2, v33
	v_fmamk_f32 v2, v2, 0x3c000000, v188
	v_rsq_f32_e32 v2, v2
	s_nop 0
	v_mul_f32_e32 v49, 0x3f24fd5c, v2
	s_nop 1
	v_add_f32_dpp v2, v80, v80 quad_perm:[1,0,3,2] row_mask:0xf bank_mask:0xf
	s_nop 1
	v_add_f32_dpp v2, v2, v2 quad_perm:[2,3,0,1] row_mask:0xf bank_mask:0xf
	s_nop 1
	v_add_f32_dpp v2, v2, v2 row_half_mirror row_mask:0xf bank_mask:0xf
	s_nop 1
	v_add_f32_dpp v2, v2, v2 row_mirror row_mask:0xf bank_mask:0xf
	v_mov_b32_e32 v33, v2
	s_nop 1
	v_permlane16_swap_b32_e32 v2, v33
	v_add_f32_e32 v2, v2, v33
	s_waitcnt lgkmcnt(0)
	s_nop 0
	s_nop 0
	s_nop 0
	v_fmamk_f32 v2, v2, 0x3c000000, v188
	v_rsq_f32_e32 v2, v2
	s_nop 0
	v_mul_f32_e32 v63, 0x3f24fd5c, v2
	s_nop 1
	v_add_f32_dpp v2, v81, v81 quad_perm:[1,0,3,2] row_mask:0xf bank_mask:0xf
	s_nop 1
	v_add_f32_dpp v2, v2, v2 quad_perm:[2,3,0,1] row_mask:0xf bank_mask:0xf
	s_nop 1
	v_add_f32_dpp v2, v2, v2 row_half_mirror row_mask:0xf bank_mask:0xf
	s_nop 1
	v_add_f32_dpp v2, v2, v2 row_mirror row_mask:0xf bank_mask:0xf
	v_mov_b32_e32 v33, v2
	s_nop 1
	v_permlane16_swap_b32_e32 v2, v33
	v_add_f32_e32 v2, v2, v33
	s_waitcnt lgkmcnt(0)
	s_nop 0
	s_nop 0
	s_nop 0
	v_fmamk_f32 v2, v2, 0x3c000000, v188
	v_rsq_f32_e32 v2, v2
	s_nop 0
	v_mul_f32_e32 v62, 0x3f24fd5c, v2
	s_nop 1
	v_add_f32_dpp v2, v87, v87 quad_perm:[1,0,3,2] row_mask:0xf bank_mask:0xf
	s_nop 1
	v_add_f32_dpp v2, v2, v2 quad_perm:[2,3,0,1] row_mask:0xf bank_mask:0xf
	s_nop 1
	v_add_f32_dpp v2, v2, v2 row_half_mirror row_mask:0xf bank_mask:0xf
	s_nop 1
	v_add_f32_dpp v2, v2, v2 row_mirror row_mask:0xf bank_mask:0xf
	v_mov_b32_e32 v33, v2
	s_nop 1
	v_permlane16_swap_b32_e32 v2, v33
	v_add_f32_e32 v2, v2, v33
	s_waitcnt lgkmcnt(0)
	s_nop 0
	s_nop 0
	s_nop 0
	v_fmamk_f32 v2, v2, 0x3c000000, v188
	v_rsq_f32_e32 v2, v2
	s_nop 0
	v_mul_f32_e32 v64, 0x3f24fd5c, v2
	s_nop 1
	v_add_f32_dpp v2, v88, v88 quad_perm:[1,0,3,2] row_mask:0xf bank_mask:0xf
	s_nop 1
	v_add_f32_dpp v2, v2, v2 quad_perm:[2,3,0,1] row_mask:0xf bank_mask:0xf
	s_nop 1
	v_add_f32_dpp v2, v2, v2 row_half_mirror row_mask:0xf bank_mask:0xf
	s_nop 1
	v_add_f32_dpp v2, v2, v2 row_mirror row_mask:0xf bank_mask:0xf
	v_mov_b32_e32 v33, v2
	s_nop 1
	v_permlane16_swap_b32_e32 v2, v33
	v_add_f32_e32 v2, v2, v33
	s_waitcnt lgkmcnt(0)
; __device__ __forceinline__ float half_sum32(float v) { v += swz_xor_f<1>(v); v += swz_xor_f<2>(v); v += swz_xor_f<4>(v); v += swz_xor_f<8>(v); v += swz_xor_f<16>(v); return v; }
; __device__ __forceinline__ void attn_unit_f8(const bf16_t* __restrict__ Q, const bf16_t* __restrict__ Kb, const unsigned char* __restrict__ V8, bf16_t* __restrict__ O, ...
;     ...
;     for (int r = 0; r < 16; ++r) { float s = half_sum32(ss[r]); ss[r] = __builtin_amdgcn_rsqf(s * (1.0f / 128.0f) + LN_EPS) * (1.0f - LAM_INIT); }
;     float gsub[4];
; #pragma unroll
;     for (int d0 = 0; d0 < 4; ++d0) gsub[d0] = subg[d0 * 32 + r32];
	s_nop 0
	s_nop 0
	s_nop 0
	v_fmamk_f32 v2, v2, 0x3c000000, v188
	v_rsq_f32_e32 v2, v2
	s_nop 0
	v_mul_f32_e32 v65, 0x3f24fd5c, v2
	s_nop 1
	v_add_f32_dpp v2, v89, v89 quad_perm:[1,0,3,2] row_mask:0xf bank_mask:0xf
	s_nop 1
	v_add_f32_dpp v2, v2, v2 quad_perm:[2,3,0,1] row_mask:0xf bank_mask:0xf
	s_nop 1
	v_add_f32_dpp v2, v2, v2 row_half_mirror row_mask:0xf bank_mask:0xf
	s_nop 1
	v_add_f32_dpp v2, v2, v2 row_mirror row_mask:0xf bank_mask:0xf
	v_mov_b32_e32 v33, v2
	s_nop 1
	v_permlane16_swap_b32_e32 v2, v33
	v_add_f32_e32 v2, v2, v33
	s_waitcnt lgkmcnt(0)
	s_nop 0
	s_nop 0
	s_nop 0
	v_fmamk_f32 v2, v2, 0x3c000000, v188
	v_rsq_f32_e32 v2, v2
	s_nop 0
	v_mul_f32_e32 v79, 0x3f24fd5c, v2
	s_nop 1
	v_add_f32_dpp v2, v82, v82 quad_perm:[1,0,3,2] row_mask:0xf bank_mask:0xf
	s_nop 1
	v_add_f32_dpp v2, v2, v2 quad_perm:[2,3,0,1] row_mask:0xf bank_mask:0xf
	s_nop 1
	v_add_f32_dpp v2, v2, v2 row_half_mirror row_mask:0xf bank_mask:0xf
	s_nop 1
	v_add_f32_dpp v2, v2, v2 row_mirror row_mask:0xf bank_mask:0xf
	v_mov_b32_e32 v33, v2
	s_nop 1
	v_permlane16_swap_b32_e32 v2, v33
	v_add_f32_e32 v2, v2, v33
	s_waitcnt lgkmcnt(0)
	s_nop 0
	s_nop 0
	s_nop 0
	v_fmamk_f32 v2, v2, 0x3c000000, v188
	v_rsq_f32_e32 v2, v2
	s_nop 0
	v_mul_f32_e32 v78, 0x3f24fd5c, v2
	s_nop 1
	v_add_f32_dpp v2, v83, v83 quad_perm:[1,0,3,2] row_mask:0xf bank_mask:0xf
	s_nop 1
	v_add_f32_dpp v2, v2, v2 quad_perm:[2,3,0,1] row_mask:0xf bank_mask:0xf
	s_nop 1
	v_add_f32_dpp v2, v2, v2 row_half_mirror row_mask:0xf bank_mask:0xf
	s_nop 1
	v_add_f32_dpp v2, v2, v2 row_mirror row_mask:0xf bank_mask:0xf
	v_mov_b32_e32 v33, v2
	s_nop 1
	v_permlane16_swap_b32_e32 v2, v33
	v_add_f32_e32 v2, v2, v33
	s_waitcnt lgkmcnt(0)
	s_nop 0
	s_nop 0
	s_nop 0
	v_fmamk_f32 v2, v2, 0x3c000000, v188
	v_rsq_f32_e32 v2, v2
	s_nop 0
	v_mul_f32_e32 v80, 0x3f24fd5c, v2
	s_nop 1
	v_add_f32_dpp v2, v84, v84 quad_perm:[1,0,3,2] row_mask:0xf bank_mask:0xf
	s_nop 1
	v_add_f32_dpp v2, v2, v2 quad_perm:[2,3,0,1] row_mask:0xf bank_mask:0xf
	s_nop 1
	v_add_f32_dpp v2, v2, v2 row_half_mirror row_mask:0xf bank_mask:0xf
	s_nop 1
	v_add_f32_dpp v2, v2, v2 row_mirror row_mask:0xf bank_mask:0xf
	v_mov_b32_e32 v33, v2
	s_nop 1
	v_permlane16_swap_b32_e32 v2, v33
	v_add_f32_e32 v2, v2, v33
	s_waitcnt lgkmcnt(0)
	s_nop 0
	s_nop 0
	s_nop 0
	v_fmamk_f32 v2, v2, 0x3c000000, v188
	v_rsq_f32_e32 v2, v2
	s_nop 0
	v_mul_f32_e32 v84, 0x3f24fd5c, v2
	ds_swizzle_b32 v2, v3 offset:swizzle(SWAP,1)
	s_waitcnt lgkmcnt(0)
	v_add_f32_e32 v2, v3, v2
	ds_swizzle_b32 v3, v2 offset:swizzle(SWAP,2)
	s_waitcnt lgkmcnt(0)
	v_add_f32_e32 v2, v2, v3
	ds_swizzle_b32 v3, v2 offset:swizzle(SWAP,4)
	s_waitcnt lgkmcnt(0)
	v_add_f32_e32 v2, v2, v3
	ds_swizzle_b32 v3, v2 offset:swizzle(SWAP,8)
	s_waitcnt lgkmcnt(0)
	v_add_f32_e32 v2, v2, v3
	ds_swizzle_b32 v3, v2 offset:swizzle(SWAP,16)
	s_waitcnt lgkmcnt(0)
	v_add_f32_e32 v2, v2, v3
	v_fmamk_f32 v2, v2, 0x3c000000, v188
	v_rsq_f32_e32 v2, v2
	s_nop 0
	v_mul_f32_e32 v81, 0x3f24fd5c, v2
	s_nop 1
	v_add_f32_dpp v2, v85, v85 quad_perm:[1,0,3,2] row_mask:0xf bank_mask:0xf
	s_nop 1
	v_add_f32_dpp v2, v2, v2 quad_perm:[2,3,0,1] row_mask:0xf bank_mask:0xf
	s_nop 1
	v_add_f32_dpp v2, v2, v2 row_half_mirror row_mask:0xf bank_mask:0xf
	s_nop 1
	v_add_f32_dpp v2, v2, v2 row_mirror row_mask:0xf bank_mask:0xf
	v_mov_b32_e32 v3, v2
	s_nop 1
	v_permlane16_swap_b32_e32 v2, v3
	v_add_f32_e32 v2, v2, v3
	s_waitcnt lgkmcnt(0)
	s_nop 0
	s_nop 0
	s_nop 0
	v_fmamk_f32 v2, v2, 0x3c000000, v188
	v_rsq_f32_e32 v2, v2
	s_nop 0
	v_mul_f32_e32 v82, 0x3f24fd5c, v2
	ds_swizzle_b32 v2, v86 offset:swizzle(SWAP,1)
	s_waitcnt lgkmcnt(0)
	v_add_f32_e32 v2, v86, v2
	ds_swizzle_b32 v3, v2 offset:swizzle(SWAP,2)
	global_load_dword v85, v77, s[4:5]
	global_load_dword v87, v77, s[4:5] offset:128
	global_load_dword v86, v77, s[4:5] offset:256
	s_nop 0
	global_load_dword v77, v77, s[4:5] offset:384
	s_waitcnt lgkmcnt(0)
	v_add_f32_e32 v2, v2, v3
	ds_swizzle_b32 v3, v2 offset:swizzle(SWAP,4)
	s_waitcnt lgkmcnt(0)
	v_add_f32_e32 v2, v2, v3
	ds_swizzle_b32 v3, v2 offset:swizzle(SWAP,8)
	s_waitcnt lgkmcnt(0)
	v_add_f32_e32 v2, v2, v3
	ds_swizzle_b32 v3, v2 offset:swizzle(SWAP,16)
	s_waitcnt lgkmcnt(0)
	v_add_f32_e32 v2, v2, v3
	v_fmamk_f32 v2, v2, 0x3c000000, v188
	v_rsq_f32_e32 v2, v2
	s_nop 0
	v_mul_f32_e32 v83, 0x3f24fd5c, v2
	s_nop 1
	v_add_f32_dpp v2, v92, v92 quad_perm:[1,0,3,2] row_mask:0xf bank_mask:0xf
	s_nop 1
	v_add_f32_dpp v2, v2, v2 quad_perm:[2,3,0,1] row_mask:0xf bank_mask:0xf
	s_nop 1
	v_add_f32_dpp v2, v2, v2 row_half_mirror row_mask:0xf bank_mask:0xf
	s_nop 1
	v_add_f32_dpp v2, v2, v2 row_mirror row_mask:0xf bank_mask:0xf
	v_mov_b32_e32 v3, v2
	s_nop 1
	v_permlane16_swap_b32_e32 v2, v3
	v_add_f32_e32 v2, v2, v3
	s_waitcnt lgkmcnt(0)
	s_nop 0
	s_nop 0
	s_nop 0
	v_fmamk_f32 v2, v2, 0x3c000000, v188
	v_rsq_f32_e32 v2, v2
	s_nop 0
	v_mul_f32_e32 v48, 0x3f24fd5c, v2
	s_nop 1
	v_add_f32_dpp v2, v93, v93 quad_perm:[1,0,3,2] row_mask:0xf bank_mask:0xf
	s_nop 1
	v_add_f32_dpp v2, v2, v2 quad_perm:[2,3,0,1] row_mask:0xf bank_mask:0xf
	s_nop 1
	v_add_f32_dpp v2, v2, v2 row_half_mirror row_mask:0xf bank_mask:0xf
	s_nop 1
	v_add_f32_dpp v2, v2, v2 row_mirror row_mask:0xf bank_mask:0xf
	v_mov_b32_e32 v3, v2
	s_nop 1
	v_permlane16_swap_b32_e32 v2, v3
	v_add_f32_e32 v2, v2, v3
	s_waitcnt lgkmcnt(0)
	s_nop 0
	s_nop 0
	s_nop 0
	v_fmamk_f32 v2, v2, 0x3c000000, v188
	v_rsq_f32_e32 v2, v2
	s_nop 0
	v_mul_f32_e32 v47, 0x3f24fd5c, v2
	s_nop 1
	v_add_f32_dpp v2, v90, v90 quad_perm:[1,0,3,2] row_mask:0xf bank_mask:0xf
	s_nop 1
	v_add_f32_dpp v2, v2, v2 quad_perm:[2,3,0,1] row_mask:0xf bank_mask:0xf
	s_nop 1
	v_add_f32_dpp v2, v2, v2 row_half_mirror row_mask:0xf bank_mask:0xf
	s_nop 1
	v_add_f32_dpp v2, v2, v2 row_mirror row_mask:0xf bank_mask:0xf
	v_mov_b32_e32 v3, v2
	s_nop 1
	v_permlane16_swap_b32_e32 v2, v3
	v_add_f32_e32 v2, v2, v3
	s_waitcnt lgkmcnt(0)
; __device__ __forceinline__ unsigned cvt_fp8x4(float a, float b, float c, float d) { int w = __builtin_amdgcn_cvt_pk_fp8_f32(a, b, 0, false); w = __builtin_amdgcn_cvt_pk_fp8_f32(c, d, w, true); return (unsigned)w; }
; __device__ __forceinline__ float half_sum32(float v) { v += swz_xor_f<1>(v); v += swz_xor_f<2>(v); v += swz_xor_f<4>(v); v += swz_xor_f<8>(v); v += swz_xor_f<16>(v); return v; }
; __device__ __forceinline__ int crow(int r, int hi) { return (r & 3) + 8 * (r >> 2) + 4 * hi; }
; __device__ __forceinline__ void attn_unit_f8(const bf16_t* __restrict__ Q, const bf16_t* __restrict__ Kb, const unsigned char* __restrict__ V8, bf16_t* __restrict__ O, ...
;     ...
;     for (int r = 0; r < 16; ++r) { float s = half_sum32(ss[r]); ss[r] = __builtin_amdgcn_rsqf(s * (1.0f / 128.0f) + LN_EPS) * (1.0f - LAM_INIT); }
;     float gsub[4];
; #pragma unroll
;     for (int d0 = 0; d0 < 4; ++d0) gsub[d0] = subg[d0 * 32 + r32];
;     unsigned char* Ow = (unsigned char*)O + (size_t)(qrow0 + wq * QBLK) * DM + h * 128;
; #pragma unroll
;     for (int r = 0; r < 16; ++r) { const int orow = crow(r, hi);
; #pragma unroll
;       for (int d0 = 0; d0 < 4; ++d0) Ow[(size_t)orow * DM + d0 * 32 + r32] = (unsigned char)(cvt_fp8x4(o[d0][r] * ss[r] * gsub[d0], 0.f, 0.f, 0.f) & 0xffu); }
	s_nop 0
	s_nop 0
	s_nop 0
	v_fmamk_f32 v2, v2, 0x3c000000, v188
	v_rsq_f32_e32 v2, v2
	s_nop 0
	v_mul_f32_e32 v33, 0x3f24fd5c, v2
	s_nop 1
	v_add_f32_dpp v2, v17, v17 quad_perm:[1,0,3,2] row_mask:0xf bank_mask:0xf
	s_nop 1
	v_add_f32_dpp v2, v2, v2 quad_perm:[2,3,0,1] row_mask:0xf bank_mask:0xf
	s_nop 1
	v_add_f32_dpp v2, v2, v2 row_half_mirror row_mask:0xf bank_mask:0xf
	s_nop 1
	v_add_f32_dpp v2, v2, v2 row_mirror row_mask:0xf bank_mask:0xf
	v_mov_b32_e32 v3, v2
	s_nop 1
	v_permlane16_swap_b32_e32 v2, v3
	v_add_f32_e32 v2, v2, v3
	s_waitcnt lgkmcnt(0)
	s_nop 0
	s_nop 0
	s_nop 0
	v_fmamk_f32 v2, v2, 0x3c000000, v188
	v_rsq_f32_e32 v2, v2
	s_nop 0
	v_mul_f32_e32 v17, 0x3f24fd5c, v2
	v_lshl_add_u64 v[2:3], s[0:1], 0, v[178:179]
	v_lshl_add_u64 v[2:3], v[2:3], 0, v[0:1]
	v_mul_f32_e32 v0, v66, v49
	s_waitcnt vmcnt(3)
	v_mul_f32_e32 v0, v0, v85
	v_mov_b32_e32 v66, v1
	v_cvt_pk_fp8_f32 v66, v0, 0
	v_mul_f32_e32 v0, v18, v49
	s_waitcnt vmcnt(2)
	v_mul_f32_e32 v0, v0, v87
	v_mov_b32_e32 v18, v1
	v_cvt_pk_fp8_f32 v18, v0, 0
	v_mul_f32_e32 v0, v67, v49
	s_waitcnt vmcnt(1)
	v_mul_f32_e32 v0, v0, v86
	s_movk_i32 s0, 0x2000
	v_cvt_pk_fp8_f32 v18, 0, 0 op_sel:[0,0,1]
	v_cvt_pk_fp8_f32 v66, 0, 0 op_sel:[0,0,1]
	global_store_byte v[2:3], v18, off offset:32
	v_mov_b32_e32 v18, v1
	v_cvt_pk_fp8_f32 v18, v0, 0
	v_mul_f32_e32 v0, v34, v49
	s_waitcnt vmcnt(1)
	v_mul_f32_e32 v0, v0, v77
	global_store_byte v[2:3], v66, off
	v_cvt_pk_fp8_f32 v18, 0, 0 op_sel:[0,0,1]
	global_store_byte v[2:3], v18, off offset:64
	v_mov_b32_e32 v18, v1
	v_cvt_pk_fp8_f32 v18, v0, 0
	v_mul_f32_e32 v0, v50, v63
	v_mul_f32_e32 v0, v0, v85
	v_cvt_pk_fp8_f32 v18, 0, 0 op_sel:[0,0,1]
	global_store_byte v[2:3], v18, off offset:96
	v_mov_b32_e32 v18, v1
	v_cvt_pk_fp8_f32 v18, v0, 0
	v_mul_f32_e32 v0, v19, v63
	v_mul_f32_e32 v0, v0, v87
	v_cvt_pk_fp8_f32 v18, 0, 0 op_sel:[0,0,1]
	global_store_byte v[2:3], v18, off offset:1024
	v_mov_b32_e32 v18, v1
	v_cvt_pk_fp8_f32 v18, v0, 0
	v_mul_f32_e32 v0, v68, v63
	v_mul_f32_e32 v0, v0, v86
	v_cvt_pk_fp8_f32 v18, 0, 0 op_sel:[0,0,1]
	global_store_byte v[2:3], v18, off offset:1056
	v_mov_b32_e32 v18, v1
	v_cvt_pk_fp8_f32 v18, v0, 0
	v_mul_f32_e32 v0, v35, v63
	v_mul_f32_e32 v0, v0, v77
	v_cvt_pk_fp8_f32 v18, 0, 0 op_sel:[0,0,1]
	global_store_byte v[2:3], v18, off offset:1088
	v_mov_b32_e32 v18, v1
	v_cvt_pk_fp8_f32 v18, v0, 0
	v_mul_f32_e32 v0, v51, v62
	v_mul_f32_e32 v0, v0, v85
	v_cvt_pk_fp8_f32 v18, 0, 0 op_sel:[0,0,1]
	global_store_byte v[2:3], v18, off offset:1120
	v_mov_b32_e32 v18, v1
	v_cvt_pk_fp8_f32 v18, v0, 0
	v_mul_f32_e32 v0, v4, v62
	v_mul_f32_e32 v0, v0, v87
	v_mov_b32_e32 v4, v1
	v_cvt_pk_fp8_f32 v4, v0, 0
	v_mul_f32_e32 v0, v69, v62
	v_mul_f32_e32 v0, v0, v86
	v_cvt_pk_fp8_f32 v18, 0, 0 op_sel:[0,0,1]
	v_cvt_pk_fp8_f32 v4, 0, 0 op_sel:[0,0,1]
	global_store_byte v[2:3], v18, off offset:2048
	global_store_byte v[2:3], v4, off offset:2080
	v_mov_b32_e32 v4, v1
	v_cvt_pk_fp8_f32 v4, v0, 0
	v_mul_f32_e32 v0, v36, v62
	v_mul_f32_e32 v0, v0, v77
	v_mov_b32_e32 v18, v1
	v_cvt_pk_fp8_f32 v4, 0, 0 op_sel:[0,0,1]
	global_store_byte v[2:3], v4, off offset:2112
	v_mov_b32_e32 v4, v1
	v_cvt_pk_fp8_f32 v4, v0, 0
	v_mul_f32_e32 v0, v52, v64
	v_mul_f32_e32 v0, v0, v85
	v_cvt_pk_fp8_f32 v4, 0, 0 op_sel:[0,0,1]
	global_store_byte v[2:3], v4, off offset:2144
	v_mov_b32_e32 v4, v1
	v_cvt_pk_fp8_f32 v4, v0, 0
	v_mul_f32_e32 v0, v5, v64
	v_mul_f32_e32 v0, v0, v87
	v_cvt_pk_fp8_f32 v4, 0, 0 op_sel:[0,0,1]
	global_store_byte v[2:3], v4, off offset:3072
	v_mov_b32_e32 v4, v1
	v_cvt_pk_fp8_f32 v4, v0, 0
	v_mul_f32_e32 v0, v70, v64
	v_mul_f32_e32 v0, v0, v86
	v_cvt_pk_fp8_f32 v4, 0, 0 op_sel:[0,0,1]
	global_store_byte v[2:3], v4, off offset:3104
	v_mov_b32_e32 v4, v1
	v_cvt_pk_fp8_f32 v4, v0, 0
	v_mul_f32_e32 v0, v21, v64
	v_mul_f32_e32 v0, v0, v77
	v_cvt_pk_fp8_f32 v4, 0, 0 op_sel:[0,0,1]
	global_store_byte v[2:3], v4, off offset:3136
	v_mov_b32_e32 v4, v1
	v_cvt_pk_fp8_f32 v4, v0, 0
	v_mul_f32_e32 v0, v53, v65
	v_mul_f32_e32 v0, v0, v85
	v_cvt_pk_fp8_f32 v18, v0, 0
	v_cvt_pk_fp8_f32 v4, 0, 0 op_sel:[0,0,1]
	v_mul_f32_e32 v0, v20, v65
	v_mul_f32_e32 v0, v0, v87
	v_cvt_pk_fp8_f32 v18, 0, 0 op_sel:[0,0,1]
	global_store_byte v[2:3], v4, off offset:3168
	v_add_co_u32_e32 v4, vcc, s0, v2
	s_movk_i32 s0, 0x4000
	s_nop 0
	v_addc_co_u32_e32 v5, vcc, 0, v3, vcc
	global_store_byte v[4:5], v18, off
	v_mov_b32_e32 v18, v1
	v_cvt_pk_fp8_f32 v18, v0, 0
	v_mul_f32_e32 v0, v38, v65
	v_mul_f32_e32 v0, v0, v86
	v_cvt_pk_fp8_f32 v18, 0, 0 op_sel:[0,0,1]
	global_store_byte v[4:5], v18, off offset:32
	v_mov_b32_e32 v18, v1
	v_cvt_pk_fp8_f32 v18, v0, 0
	v_mul_f32_e32 v0, v22, v65
	v_mul_f32_e32 v0, v0, v77
	v_cvt_pk_fp8_f32 v18, 0, 0 op_sel:[0,0,1]
	global_store_byte v[4:5], v18, off offset:64
	v_mov_b32_e32 v18, v1
	v_cvt_pk_fp8_f32 v18, v0, 0
	v_mul_f32_e32 v0, v54, v79
	v_mul_f32_e32 v0, v0, v85
	v_cvt_pk_fp8_f32 v18, 0, 0 op_sel:[0,0,1]
	global_store_byte v[4:5], v18, off offset:96
	v_mov_b32_e32 v18, v1
	v_cvt_pk_fp8_f32 v18, v0, 0
	v_mul_f32_e32 v0, v7, v79
	v_mul_f32_e32 v0, v0, v87
	v_mov_b32_e32 v7, v1
	v_cvt_pk_fp8_f32 v7, v0, 0
	v_mul_f32_e32 v0, v71, v79
	v_mul_f32_e32 v0, v0, v86
	v_cvt_pk_fp8_f32 v18, 0, 0 op_sel:[0,0,1]
	v_cvt_pk_fp8_f32 v7, 0, 0 op_sel:[0,0,1]
	global_store_byte v[4:5], v18, off offset:1024
	global_store_byte v[4:5], v7, off offset:1056
	v_mov_b32_e32 v7, v1
	v_cvt_pk_fp8_f32 v7, v0, 0
	v_mul_f32_e32 v0, v37, v79
	v_mul_f32_e32 v0, v0, v77
	v_cvt_pk_fp8_f32 v7, 0, 0 op_sel:[0,0,1]
	global_store_byte v[4:5], v7, off offset:1088
	v_mov_b32_e32 v7, v1
	v_cvt_pk_fp8_f32 v7, v0, 0
	v_mul_f32_e32 v0, v55, v78
	v_mul_f32_e32 v0, v0, v85
; __device__ __forceinline__ unsigned cvt_fp8x4(float a, float b, float c, float d) { int w = __builtin_amdgcn_cvt_pk_fp8_f32(a, b, 0, false); w = __builtin_amdgcn_cvt_pk_fp8_f32(c, d, w, true); return (unsigned)w; }
; __device__ __forceinline__ int crow(int r, int hi) { return (r & 3) + 8 * (r >> 2) + 4 * hi; }
; __device__ __forceinline__ void attn_unit_f8(const bf16_t* __restrict__ Q, const bf16_t* __restrict__ Kb, const unsigned char* __restrict__ V8, bf16_t* __restrict__ O, ...
;     ...
;     unsigned char* Ow = (unsigned char*)O + (size_t)(qrow0 + wq * QBLK) * DM + h * 128;
; #pragma unroll
;     for (int r = 0; r < 16; ++r) { const int orow = crow(r, hi);
; #pragma unroll
;       for (int d0 = 0; d0 < 4; ++d0) Ow[(size_t)orow * DM + d0 * 32 + r32] = (unsigned char)(cvt_fp8x4(o[d0][r] * ss[r] * gsub[d0], 0.f, 0.f, 0.f) & 0xffu); }
	v_cvt_pk_fp8_f32 v7, 0, 0 op_sel:[0,0,1]
	global_store_byte v[4:5], v7, off offset:1120
	v_mov_b32_e32 v7, v1
	v_cvt_pk_fp8_f32 v7, v0, 0
	v_mul_f32_e32 v0, v23, v78
	v_mul_f32_e32 v0, v0, v87
	v_cvt_pk_fp8_f32 v7, 0, 0 op_sel:[0,0,1]
	global_store_byte v[4:5], v7, off offset:2048
	v_mov_b32_e32 v7, v1
	v_cvt_pk_fp8_f32 v7, v0, 0
	v_mul_f32_e32 v0, v72, v78
	v_mul_f32_e32 v0, v0, v86
	v_cvt_pk_fp8_f32 v7, 0, 0 op_sel:[0,0,1]
	global_store_byte v[4:5], v7, off offset:2080
	v_mov_b32_e32 v7, v1
	v_cvt_pk_fp8_f32 v7, v0, 0
	v_mul_f32_e32 v0, v24, v78
	v_mul_f32_e32 v0, v0, v77
	v_cvt_pk_fp8_f32 v7, 0, 0 op_sel:[0,0,1]
	global_store_byte v[4:5], v7, off offset:2112
	v_mov_b32_e32 v7, v1
	v_cvt_pk_fp8_f32 v7, v0, 0
	v_mul_f32_e32 v0, v56, v80
	v_mul_f32_e32 v0, v0, v85
	v_cvt_pk_fp8_f32 v7, 0, 0 op_sel:[0,0,1]
	global_store_byte v[4:5], v7, off offset:2144
	v_mov_b32_e32 v7, v1
	v_cvt_pk_fp8_f32 v7, v0, 0
	v_mul_f32_e32 v0, v9, v80
	v_mul_f32_e32 v0, v0, v87
	v_cvt_pk_fp8_f32 v7, 0, 0 op_sel:[0,0,1]
	global_store_byte v[4:5], v7, off offset:3072
	v_mov_b32_e32 v7, v1
	v_cvt_pk_fp8_f32 v7, v0, 0
	v_mul_f32_e32 v0, v41, v80
	v_mul_f32_e32 v0, v0, v86
	v_cvt_pk_fp8_f32 v7, 0, 0 op_sel:[0,0,1]
	global_store_byte v[4:5], v7, off offset:3104
	v_mov_b32_e32 v7, v1
	v_cvt_pk_fp8_f32 v7, v0, 0
	v_mul_f32_e32 v0, v39, v80
	v_mul_f32_e32 v0, v0, v77
	v_cvt_pk_fp8_f32 v7, 0, 0 op_sel:[0,0,1]
	global_store_byte v[4:5], v7, off offset:3136
	v_mov_b32_e32 v7, v1
	v_cvt_pk_fp8_f32 v7, v0, 0
	v_mul_f32_e32 v0, v73, v84
	v_mul_f32_e32 v0, v0, v85
	v_cvt_pk_fp8_f32 v7, 0, 0 op_sel:[0,0,1]
	global_store_byte v[4:5], v7, off offset:3168
	v_mov_b32_e32 v7, v1
	v_cvt_pk_fp8_f32 v7, v0, 0
	v_add_co_u32_e32 v4, vcc, s0, v2
	v_mul_f32_e32 v0, v10, v84
	v_cvt_pk_fp8_f32 v7, 0, 0 op_sel:[0,0,1]
	v_addc_co_u32_e32 v5, vcc, 0, v3, vcc
	v_mul_f32_e32 v0, v0, v87
	global_store_byte v[4:5], v7, off
	v_mov_b32_e32 v7, v1
	v_cvt_pk_fp8_f32 v7, v0, 0
	v_mul_f32_e32 v0, v57, v84
	v_mul_f32_e32 v0, v0, v86
	s_movk_i32 s0, 0x6000
	v_cvt_pk_fp8_f32 v7, 0, 0 op_sel:[0,0,1]
	v_add_co_u32_e32 v2, vcc, s0, v2
	global_store_byte v[4:5], v7, off offset:32
	v_mov_b32_e32 v7, v1
	v_cvt_pk_fp8_f32 v7, v0, 0
	v_mul_f32_e32 v0, v26, v84
	v_mul_f32_e32 v0, v0, v77
	v_addc_co_u32_e32 v3, vcc, 0, v3, vcc
	v_cvt_pk_fp8_f32 v7, 0, 0 op_sel:[0,0,1]
	global_store_byte v[4:5], v7, off offset:64
	v_mov_b32_e32 v7, v1
	v_cvt_pk_fp8_f32 v7, v0, 0
	v_mul_f32_e32 v0, v58, v81
	v_mul_f32_e32 v0, v0, v85
	v_cvt_pk_fp8_f32 v7, 0, 0 op_sel:[0,0,1]
	global_store_byte v[4:5], v7, off offset:96
	v_mov_b32_e32 v7, v1
	v_cvt_pk_fp8_f32 v7, v0, 0
	v_mul_f32_e32 v0, v25, v81
	v_mul_f32_e32 v0, v0, v87
	v_cvt_pk_fp8_f32 v7, 0, 0 op_sel:[0,0,1]
	global_store_byte v[4:5], v7, off offset:1024
	v_mov_b32_e32 v7, v1
	v_cvt_pk_fp8_f32 v7, v0, 0
	v_mul_f32_e32 v0, v74, v81
	v_mul_f32_e32 v0, v0, v86
	v_cvt_pk_fp8_f32 v7, 0, 0 op_sel:[0,0,1]
	global_store_byte v[4:5], v7, off offset:1056
	v_mov_b32_e32 v7, v1
	v_cvt_pk_fp8_f32 v7, v0, 0
	v_mul_f32_e32 v0, v40, v81
	v_mul_f32_e32 v0, v0, v77
	v_cvt_pk_fp8_f32 v7, 0, 0 op_sel:[0,0,1]
	global_store_byte v[4:5], v7, off offset:1088
	v_mov_b32_e32 v7, v1
	v_cvt_pk_fp8_f32 v7, v0, 0
	v_mul_f32_e32 v0, v59, v82
	v_mul_f32_e32 v0, v0, v85
	v_cvt_pk_fp8_f32 v7, 0, 0 op_sel:[0,0,1]
	global_store_byte v[4:5], v7, off offset:1120
	v_mov_b32_e32 v7, v1
	v_cvt_pk_fp8_f32 v7, v0, 0
	v_mul_f32_e32 v0, v27, v82
	v_mul_f32_e32 v0, v0, v87
	v_cvt_pk_fp8_f32 v7, 0, 0 op_sel:[0,0,1]
	global_store_byte v[4:5], v7, off offset:2048
	v_mov_b32_e32 v7, v1
	v_cvt_pk_fp8_f32 v7, v0, 0
	v_mul_f32_e32 v0, v75, v82
	v_mul_f32_e32 v0, v0, v86
	v_cvt_pk_fp8_f32 v7, 0, 0 op_sel:[0,0,1]
	global_store_byte v[4:5], v7, off offset:2080
	v_mov_b32_e32 v7, v1
	v_cvt_pk_fp8_f32 v7, v0, 0
	v_mul_f32_e32 v0, v42, v82
	v_mul_f32_e32 v0, v0, v77
	v_cvt_pk_fp8_f32 v7, 0, 0 op_sel:[0,0,1]
	global_store_byte v[4:5], v7, off offset:2112
	v_mov_b32_e32 v7, v1
	v_cvt_pk_fp8_f32 v7, v0, 0
; __device__ __forceinline__ unsigned cvt_fp8x4(float a, float b, float c, float d) { int w = __builtin_amdgcn_cvt_pk_fp8_f32(a, b, 0, false); w = __builtin_amdgcn_cvt_pk_fp8_f32(c, d, w, true); return (unsigned)w; }
; __device__ __forceinline__ int crow(int r, int hi) { return (r & 3) + 8 * (r >> 2) + 4 * hi; }
; __device__ __forceinline__ void attn_unit_f8(const bf16_t* __restrict__ Q, const bf16_t* __restrict__ Kb, const unsigned char* __restrict__ V8, bf16_t* __restrict__ O, ...
;     ...
;     unsigned char* Ow = (unsigned char*)O + (size_t)(qrow0 + wq * QBLK) * DM + h * 128;
; #pragma unroll
;     for (int r = 0; r < 16; ++r) { const int orow = crow(r, hi);
; #pragma unroll
;       for (int d0 = 0; d0 < 4; ++d0) Ow[(size_t)orow * DM + d0 * 32 + r32] = (unsigned char)(cvt_fp8x4(o[d0][r] * ss[r] * gsub[d0], 0.f, 0.f, 0.f) & 0xffu); }
	v_mul_f32_e32 v0, v60, v83
	v_mul_f32_e32 v0, v0, v85
	v_cvt_pk_fp8_f32 v7, 0, 0 op_sel:[0,0,1]
	global_store_byte v[4:5], v7, off offset:2144
	v_mov_b32_e32 v7, v1
	v_cvt_pk_fp8_f32 v7, v0, 0
	v_mul_f32_e32 v0, v28, v83
	v_mul_f32_e32 v0, v0, v87
	v_cvt_pk_fp8_f32 v7, 0, 0 op_sel:[0,0,1]
	global_store_byte v[4:5], v7, off offset:3072
	v_mov_b32_e32 v7, v1
	v_cvt_pk_fp8_f32 v7, v0, 0
	v_mul_f32_e32 v0, v76, v83
	v_mul_f32_e32 v0, v0, v86
	v_cvt_pk_fp8_f32 v7, 0, 0 op_sel:[0,0,1]
	global_store_byte v[4:5], v7, off offset:3104
	v_mov_b32_e32 v7, v1
	v_cvt_pk_fp8_f32 v7, v0, 0
	v_mul_f32_e32 v0, v44, v83
	v_mul_f32_e32 v0, v0, v77
	v_cvt_pk_fp8_f32 v7, 0, 0 op_sel:[0,0,1]
	global_store_byte v[4:5], v7, off offset:3136
	v_mov_b32_e32 v7, v1
	v_cvt_pk_fp8_f32 v7, v0, 0
	v_mul_f32_e32 v0, v61, v48
	v_mul_f32_e32 v0, v0, v85
	v_cvt_pk_fp8_f32 v7, 0, 0 op_sel:[0,0,1]
	global_store_byte v[4:5], v7, off offset:3168
	v_mov_b32_e32 v4, v1
	v_cvt_pk_fp8_f32 v4, v0, 0
	v_mul_f32_e32 v0, v12, v48
	v_mul_f32_e32 v0, v0, v87
	v_cvt_pk_fp8_f32 v4, 0, 0 op_sel:[0,0,1]
	global_store_byte v[2:3], v4, off
	v_mov_b32_e32 v4, v1
	v_cvt_pk_fp8_f32 v4, v0, 0
	v_mul_f32_e32 v0, v45, v48
	v_mul_f32_e32 v0, v0, v86
	v_cvt_pk_fp8_f32 v4, 0, 0 op_sel:[0,0,1]
	global_store_byte v[2:3], v4, off offset:32
	v_mov_b32_e32 v4, v1
	v_cvt_pk_fp8_f32 v4, v0, 0
	v_mul_f32_e32 v0, v29, v48
	v_mul_f32_e32 v0, v0, v77
	v_cvt_pk_fp8_f32 v4, 0, 0 op_sel:[0,0,1]
	global_store_byte v[2:3], v4, off offset:64
	v_mov_b32_e32 v4, v1
	v_cvt_pk_fp8_f32 v4, v0, 0
	v_mul_f32_e32 v0, v43, v47
	v_mul_f32_e32 v0, v0, v85
	v_cvt_pk_fp8_f32 v4, 0, 0 op_sel:[0,0,1]
	global_store_byte v[2:3], v4, off offset:96
	v_mov_b32_e32 v4, v1
	v_cvt_pk_fp8_f32 v4, v0, 0
	v_mul_f32_e32 v0, v13, v47
	v_mul_f32_e32 v0, v0, v87
	v_cvt_pk_fp8_f32 v4, 0, 0 op_sel:[0,0,1]
	global_store_byte v[2:3], v4, off offset:1024
	v_mov_b32_e32 v4, v1
	v_cvt_pk_fp8_f32 v4, v0, 0
	v_mul_f32_e32 v0, v46, v47
	v_mul_f32_e32 v0, v0, v86
	v_cvt_pk_fp8_f32 v4, 0, 0 op_sel:[0,0,1]
	global_store_byte v[2:3], v4, off offset:1056
	v_mov_b32_e32 v4, v1
	v_cvt_pk_fp8_f32 v4, v0, 0
	v_mul_f32_e32 v0, v30, v47
	v_mul_f32_e32 v0, v0, v77
	v_cvt_pk_fp8_f32 v4, 0, 0 op_sel:[0,0,1]
	global_store_byte v[2:3], v4, off offset:1088
	v_mov_b32_e32 v4, v1
	v_cvt_pk_fp8_f32 v4, v0, 0
	v_mul_f32_e32 v0, v31, v33
	v_mul_f32_e32 v0, v85, v0
	v_cvt_pk_fp8_f32 v4, 0, 0 op_sel:[0,0,1]
	global_store_byte v[2:3], v4, off offset:1120
	v_mov_b32_e32 v4, v1
	v_cvt_pk_fp8_f32 v4, v0, 0
	v_mul_f32_e32 v0, v15, v33
	v_mul_f32_e32 v0, v0, v87
	v_cvt_pk_fp8_f32 v4, 0, 0 op_sel:[0,0,1]
	global_store_byte v[2:3], v4, off offset:2048
	v_mov_b32_e32 v4, v1
	v_cvt_pk_fp8_f32 v4, v0, 0
	v_mul_f32_e32 v0, v32, v33
	v_mul_f32_e32 v0, v0, v86
	v_cvt_pk_fp8_f32 v4, 0, 0 op_sel:[0,0,1]
	global_store_byte v[2:3], v4, off offset:2080
	v_mov_b32_e32 v4, v1
	v_cvt_pk_fp8_f32 v4, v0, 0
	v_mul_f32_e32 v0, v16, v33
	v_mul_f32_e32 v0, v0, v77
	v_cvt_pk_fp8_f32 v4, 0, 0 op_sel:[0,0,1]
	global_store_byte v[2:3], v4, off offset:2112
	v_mov_b32_e32 v4, v1
	v_cvt_pk_fp8_f32 v4, v0, 0
	v_mul_f32_e32 v0, v14, v17
	v_mul_f32_e32 v0, v85, v0
	v_cvt_pk_fp8_f32 v4, 0, 0 op_sel:[0,0,1]
	global_store_byte v[2:3], v4, off offset:2144
	v_mov_b32_e32 v4, v1
	v_cvt_pk_fp8_f32 v4, v0, 0
	v_mul_f32_e32 v0, v11, v17
	v_mul_f32_e32 v0, v87, v0
	v_cvt_pk_fp8_f32 v4, 0, 0 op_sel:[0,0,1]
	global_store_byte v[2:3], v4, off offset:3072
	v_mov_b32_e32 v4, v1
	v_cvt_pk_fp8_f32 v4, v0, 0
	v_mul_f32_e32 v0, v8, v17
	v_mul_f32_e32 v0, v86, v0
	v_cvt_pk_fp8_f32 v4, 0, 0 op_sel:[0,0,1]
	global_store_byte v[2:3], v4, off offset:3104
	v_mov_b32_e32 v4, v1
	v_cvt_pk_fp8_f32 v4, v0, 0
	v_mul_f32_e32 v0, v6, v17
	v_mul_f32_e32 v0, v77, v0
	v_cvt_pk_fp8_f32 v4, 0, 0 op_sel:[0,0,1]
	global_store_byte v[2:3], v4, off offset:3136
	v_mov_b32_e32 v4, v1
	v_cvt_pk_fp8_f32 v4, v0, 0
	v_cvt_pk_fp8_f32 v4, 0, 0 op_sel:[0,0,1]
	global_store_byte v[2:3], v4, off offset:3168
	s_branch .LBB0_1290
